# v28 + MLA unit prologue: the 16 QK-norm gain / rope cos-sin loads issued in front of the q_c row loads (into registers that are free until tile 0), one wait instead of a counted ladder
# baseline (speedup 1.0000x reference)
; #define LAS __attribute__((address_space(3)))
; template <bool FOX>
; __device__ __forceinline__ void attn_unit(const Args& A, int b, int h, int qb, LAS char* shm, LAS float* dg) {
;     ...
;         const long row = rowbase + qw + r32;
;         if constexpr (FOX) {
; #pragma unroll
;             for (int d0 = 0; d0 < NQ; ++d0) qr[d0] = *(const bf16x8*)(A.Fq + row * 512 + h * 64 + d0 * 16 + hi * 8);
;         } else {
;             constexpr int L_W = Lay<false>::L_W;
;             const bf16_t* qcp = A.Qc + row * 256 + hi * 8; bf16x8 qc[16];
; #pragma unroll
;             for (int s = 0; s < 16; ++s) qc[s] = *(const bf16x8*)(qcp + s * 16);
;             const f32x4 sq4 = *(const f32x4*)(A.ssq_q + row * 4);
;             f32x16 qa[3]; qa[0] = f32x16{}; qa[1] = f32x16{}; qa[2] = f32x16{};
;             const lds_cptr wp = (lds_cptr)shm + L_W + lane * 16;
; #pragma unroll
;             for (int s = 0; s < 16; ++s)
; #pragma unroll
;                 for (int blk = 0; blk < 3; ++blk) qa[blk] = __builtin_amdgcn_mfma_f32_32x32x16_bf16(*(const LAS bf16x8*)(wp + (blk * 16 + s) * 1024), qc[s], qa[blk], 0, 0, 0);
;             const float rq = rsqrtf(((sq4[0] + sq4[1]) + (sq4[2] + sq4[3])) * (1.f / 256.f) + EPS);
;             float ss = 0.f;
; #pragma unroll
;             for (int blk = 0; blk < 3; ++blk)
; #pragma unroll
;                 for (int r = 0; r < 16; ++r) ss += qa[blk][r] * qa[blk][r];
;             ss = swapsum(ss) * rq * rq;
;             const float sc = rsqrtf(ss * (1.f / 96.f) + EPS) * C2_MLA * rq;
; #pragma unroll
;             for (int blk = 0; blk < 3; ++blk)
; #pragma unroll
;                 for (int g = 0; g < 4; ++g) { const f32x4 gg = *(const f32x4*)(A.gmq + 32 * blk + 8 * g + 4 * hi);
; #pragma unroll
;                     for (int i = 0; i < 4; ++i) qa[blk][4 * g + i] *= sc * gg[i]; }
; #pragma unroll
;             for (int e = 0; e < 2; ++e) { const f32x4 c = *(const f32x4*)(A.cosT + row * 16 + 8 * e + 4 * hi), sn = *(const f32x4*)(A.sinT + row * 16 + 8 * e + 4 * hi);
; #pragma unroll
;                 for (int i = 0; i < 4; ++i) { const float x1 = qa[2][4 * e + i], x2 = qa[2][8 + 4 * e + i]; qa[2][4 * e + i] = x1 * c[i] - x2 * sn[i]; qa[2][8 + 4 * e + i] = x2 * c[i] + x1 * sn[i]; } }
.LBB0_815:
	s_lshl_b32 s26, s8, 8
	s_lshl_b32 s27, s89, 5
	s_add_i32 s27, s27, s26
	v_lshl_add_u64 v[4:5], v[100:101], 0, s[56:57]
	s_add_i32 s36, s93, 0x2000
	s_mov_b32 s37, m0
	s_mov_b32 m0, s36
	s_nop 0
	global_load_lds_dwordx4 v[4:5], off
	s_mov_b32 m0, s37
	s_ashr_i32 s37, s27, 31
	s_add_u32 s36, s30, s27
	v_and_b32_e32 v242, 31, v1
	s_addc_u32 s37, s31, s37
	v_or_b32_e32 v54, s36, v242
	v_mov_b32_e32 v55, s37
	v_lshrrev_b32_e32 v243, 5, v134
	v_lshlrev_b64 v[4:5], 9, v[54:55]
	v_lshl_add_u64 v[4:5], s[0:1], 0, v[4:5]
	v_lshlrev_b32_e32 v52, 4, v243
	v_mov_b32_e32 v53, v131
	v_lshl_add_u64 v[56:57], v[4:5], 0, v[52:53]
	v_lshlrev_b64 v[116:117], 6, v[54:55]
	v_lshl_add_u64 v[118:119], s[18:19], 0, v[116:117]
	v_lshl_add_u64 v[116:117], s[28:29], 0, v[116:117]
	v_lshl_add_u64 v[118:119], v[118:119], 0, v[52:53]
	v_lshl_add_u64 v[116:117], v[116:117], 0, v[52:53]
	global_load_dwordx4 v[162:165], v52, s[14:15]
	global_load_dwordx4 v[166:169], v52, s[14:15] offset:32
	global_load_dwordx4 v[170:173], v52, s[14:15] offset:64
	global_load_dwordx4 v[174:177], v52, s[14:15] offset:96
	global_load_dwordx4 v[178:181], v52, s[14:15] offset:128
	global_load_dwordx4 v[182:185], v52, s[14:15] offset:160
	global_load_dwordx4 v[186:189], v52, s[14:15] offset:192
	global_load_dwordx4 v[190:193], v52, s[14:15] offset:224
	global_load_dwordx4 v[194:197], v52, s[14:15] offset:256
	global_load_dwordx4 v[198:201], v52, s[14:15] offset:320
	global_load_dwordx4 v[202:205], v[116:117], off
	global_load_dwordx4 v[206:209], v[118:119], off
	global_load_dwordx4 v[210:213], v52, s[14:15] offset:352
	global_load_dwordx4 v[214:217], v52, s[14:15] offset:288
	global_load_dwordx4 v[218:221], v[116:117], off offset:32
	global_load_dwordx4 v[112:115], v[118:119], off offset:32
	global_load_dwordx4 v[4:7], v[56:57], off
	global_load_dwordx4 v[58:61], v[56:57], off offset:32
	v_lshl_add_u32 v3, v134, 4, s20
	ds_read_b128 v[8:11], v3
	ds_read_b128 v[62:65], v3 offset:1024
	s_mov_b64 s[42:43], -1
	s_waitcnt vmcnt(1) lgkmcnt(1)
	v_mfma_f32_32x32x16_bf16 v[36:51], v[8:11], v[4:7], 0
	ds_read_b128 v[8:11], v3 offset:16384
	ds_read_b128 v[66:69], v3 offset:17408
	s_waitcnt lgkmcnt(1)
	v_mfma_f32_32x32x16_bf16 v[20:35], v[8:11], v[4:7], 0
	ds_read_b128 v[8:11], v3 offset:32768
	ds_read_b128 v[70:73], v3 offset:33792
	s_waitcnt vmcnt(0)
	v_mfma_f32_32x32x16_bf16 v[36:51], v[62:65], v[58:61], v[36:51]
	global_load_dwordx4 v[62:65], v[56:57], off offset:64
	s_waitcnt lgkmcnt(1)
	v_mfma_f32_32x32x16_bf16 v[4:19], v[8:11], v[4:7], 0
	v_mfma_f32_32x32x16_bf16 v[20:35], v[66:69], v[58:61], v[20:35]
	global_load_dwordx4 v[66:69], v[56:57], off offset:96
	s_waitcnt lgkmcnt(0)
	v_mfma_f32_32x32x16_bf16 v[4:19], v[70:73], v[58:61], v[4:19]
	ds_read_b128 v[58:61], v3 offset:2048
	ds_read_b128 v[70:73], v3 offset:3072
	s_waitcnt vmcnt(1) lgkmcnt(1)
	v_mfma_f32_32x32x16_bf16 v[36:51], v[58:61], v[62:65], v[36:51]
	ds_read_b128 v[58:61], v3 offset:18432
	ds_read_b128 v[74:77], v3 offset:19456
	s_waitcnt lgkmcnt(1)
	v_mfma_f32_32x32x16_bf16 v[20:35], v[58:61], v[62:65], v[20:35]
	ds_read_b128 v[58:61], v3 offset:34816
	ds_read_b128 v[78:81], v3 offset:35840
	s_waitcnt lgkmcnt(1)
	v_mfma_f32_32x32x16_bf16 v[4:19], v[58:61], v[62:65], v[4:19]
	global_load_dwordx4 v[58:61], v[56:57], off offset:128
	global_load_dwordx4 v[62:65], v[56:57], off offset:160
	s_waitcnt vmcnt(2)
	v_mfma_f32_32x32x16_bf16 v[36:51], v[70:73], v[66:69], v[36:51]
	v_mfma_f32_32x32x16_bf16 v[20:35], v[74:77], v[66:69], v[20:35]
	s_waitcnt lgkmcnt(0)
	v_mfma_f32_32x32x16_bf16 v[4:19], v[78:81], v[66:69], v[4:19]
	ds_read_b128 v[66:69], v3 offset:4096
	ds_read_b128 v[70:73], v3 offset:5120
	s_waitcnt vmcnt(1) lgkmcnt(1)
	v_mfma_f32_32x32x16_bf16 v[36:51], v[66:69], v[58:61], v[36:51]
	ds_read_b128 v[66:69], v3 offset:20480
	ds_read_b128 v[74:77], v3 offset:21504
	s_waitcnt lgkmcnt(1)
	v_mfma_f32_32x32x16_bf16 v[20:35], v[66:69], v[58:61], v[20:35]
	ds_read_b128 v[66:69], v3 offset:36864
	ds_read_b128 v[78:81], v3 offset:37888
	s_waitcnt lgkmcnt(1)
	v_mfma_f32_32x32x16_bf16 v[4:19], v[66:69], v[58:61], v[4:19]
	global_load_dwordx4 v[58:61], v[56:57], off offset:192
	global_load_dwordx4 v[66:69], v[56:57], off offset:224
	s_waitcnt vmcnt(2)
	v_mfma_f32_32x32x16_bf16 v[36:51], v[70:73], v[62:65], v[36:51]
	v_mfma_f32_32x32x16_bf16 v[20:35], v[74:77], v[62:65], v[20:35]
	s_waitcnt lgkmcnt(0)
	v_mfma_f32_32x32x16_bf16 v[4:19], v[78:81], v[62:65], v[4:19]
	ds_read_b128 v[62:65], v3 offset:6144
	ds_read_b128 v[70:73], v3 offset:7168
	s_waitcnt vmcnt(1) lgkmcnt(1)
	v_mfma_f32_32x32x16_bf16 v[36:51], v[62:65], v[58:61], v[36:51]
	ds_read_b128 v[62:65], v3 offset:22528
	ds_read_b128 v[74:77], v3 offset:23552
	s_waitcnt lgkmcnt(1)
	v_mfma_f32_32x32x16_bf16 v[20:35], v[62:65], v[58:61], v[20:35]
	ds_read_b128 v[62:65], v3 offset:38912
	ds_read_b128 v[78:81], v3 offset:39936
	s_waitcnt lgkmcnt(1)
	v_mfma_f32_32x32x16_bf16 v[4:19], v[62:65], v[58:61], v[4:19]
	global_load_dwordx4 v[58:61], v[56:57], off offset:256
	global_load_dwordx4 v[62:65], v[56:57], off offset:288
	s_waitcnt vmcnt(2)
	v_mfma_f32_32x32x16_bf16 v[36:51], v[70:73], v[66:69], v[36:51]
	v_mfma_f32_32x32x16_bf16 v[20:35], v[74:77], v[66:69], v[20:35]
	s_waitcnt lgkmcnt(0)
	v_mfma_f32_32x32x16_bf16 v[4:19], v[78:81], v[66:69], v[4:19]
	ds_read_b128 v[66:69], v3 offset:8192
	ds_read_b128 v[70:73], v3 offset:9216
	s_waitcnt vmcnt(1) lgkmcnt(1)
	v_mfma_f32_32x32x16_bf16 v[36:51], v[66:69], v[58:61], v[36:51]
	ds_read_b128 v[66:69], v3 offset:24576
	ds_read_b128 v[74:77], v3 offset:25600
	s_waitcnt lgkmcnt(1)
; #define LAS __attribute__((address_space(3)))
; __device__ __forceinline__ float swapsum(float m) { auto rr = __builtin_amdgcn_permlane32_swap(__float_as_uint(m), __float_as_uint(m), false, false); return __uint_as_float(rr[0]) + __uint_as_float(rr[1]); }
; template <bool FOX>
; __device__ __forceinline__ void attn_unit(const Args& A, int b, int h, int qb, LAS char* shm, LAS float* dg) {
;     ...
;             const bf16_t* qcp = A.Qc + row * 256 + hi * 8; bf16x8 qc[16];
; #pragma unroll
;             for (int s = 0; s < 16; ++s) qc[s] = *(const bf16x8*)(qcp + s * 16);
;             const f32x4 sq4 = *(const f32x4*)(A.ssq_q + row * 4);
;             f32x16 qa[3]; qa[0] = f32x16{}; qa[1] = f32x16{}; qa[2] = f32x16{};
;             const lds_cptr wp = (lds_cptr)shm + L_W + lane * 16;
; #pragma unroll
;             for (int s = 0; s < 16; ++s)
; #pragma unroll
;                 for (int blk = 0; blk < 3; ++blk) qa[blk] = __builtin_amdgcn_mfma_f32_32x32x16_bf16(*(const LAS bf16x8*)(wp + (blk * 16 + s) * 1024), qc[s], qa[blk], 0, 0, 0);
;             const float rq = rsqrtf(((sq4[0] + sq4[1]) + (sq4[2] + sq4[3])) * (1.f / 256.f) + EPS);
;             float ss = 0.f;
; #pragma unroll
;             for (int blk = 0; blk < 3; ++blk)
; #pragma unroll
;                 for (int r = 0; r < 16; ++r) ss += qa[blk][r] * qa[blk][r];
;             ss = swapsum(ss) * rq * rq;
;             const float sc = rsqrtf(ss * (1.f / 96.f) + EPS) * C2_MLA * rq;
	v_mfma_f32_32x32x16_bf16 v[20:35], v[66:69], v[58:61], v[20:35]
	ds_read_b128 v[66:69], v3 offset:40960
	ds_read_b128 v[78:81], v3 offset:41984
	s_waitcnt lgkmcnt(1)
	v_mfma_f32_32x32x16_bf16 v[4:19], v[66:69], v[58:61], v[4:19]
	global_load_dwordx4 v[58:61], v[56:57], off offset:320
	global_load_dwordx4 v[66:69], v[56:57], off offset:352
	s_waitcnt vmcnt(2)
	v_mfma_f32_32x32x16_bf16 v[36:51], v[70:73], v[62:65], v[36:51]
	v_mfma_f32_32x32x16_bf16 v[20:35], v[74:77], v[62:65], v[20:35]
	s_waitcnt lgkmcnt(0)
	v_mfma_f32_32x32x16_bf16 v[4:19], v[78:81], v[62:65], v[4:19]
	ds_read_b128 v[62:65], v3 offset:10240
	ds_read_b128 v[70:73], v3 offset:11264
	s_waitcnt vmcnt(1) lgkmcnt(1)
	v_mfma_f32_32x32x16_bf16 v[36:51], v[62:65], v[58:61], v[36:51]
	ds_read_b128 v[62:65], v3 offset:26624
	ds_read_b128 v[74:77], v3 offset:27648
	s_waitcnt lgkmcnt(1)
	v_mfma_f32_32x32x16_bf16 v[20:35], v[62:65], v[58:61], v[20:35]
	ds_read_b128 v[62:65], v3 offset:43008
	ds_read_b128 v[78:81], v3 offset:44032
	s_waitcnt lgkmcnt(1)
	v_mfma_f32_32x32x16_bf16 v[4:19], v[62:65], v[58:61], v[4:19]
	global_load_dwordx4 v[58:61], v[56:57], off offset:384
	ds_read_b128 v[62:65], v3 offset:12288
	s_waitcnt vmcnt(1)
	v_mfma_f32_32x32x16_bf16 v[36:51], v[70:73], v[66:69], v[36:51]
	ds_read_b128 v[70:73], v3 offset:13312
	v_mfma_f32_32x32x16_bf16 v[20:35], v[74:77], v[66:69], v[20:35]
	v_lshl_add_u64 v[74:75], v[54:55], 4, s[12:13]
	global_load_dwordx4 v[74:77], v[74:75], off
	v_lshlrev_b64 v[54:55], 6, v[54:55]
	s_waitcnt lgkmcnt(2)
	v_mfma_f32_32x32x16_bf16 v[4:19], v[78:81], v[66:69], v[4:19]
	global_load_dwordx4 v[66:69], v[56:57], off offset:416
	s_waitcnt vmcnt(2) lgkmcnt(1)
	v_mfma_f32_32x32x16_bf16 v[36:51], v[62:65], v[58:61], v[36:51]
	ds_read_b128 v[62:65], v3 offset:28672
	ds_read_b128 v[78:81], v3 offset:45056
	ds_read_b128 v[82:85], v3 offset:29696
	ds_read_b128 v[86:89], v3 offset:46080
	s_waitcnt lgkmcnt(3)
	v_mfma_f32_32x32x16_bf16 v[20:35], v[62:65], v[58:61], v[20:35]
	global_load_dwordx4 v[62:65], v[56:57], off offset:448
	s_waitcnt lgkmcnt(2)
	v_mfma_f32_32x32x16_bf16 v[4:19], v[78:81], v[58:61], v[4:19]
	global_load_dwordx4 v[56:59], v[56:57], off offset:480
	s_waitcnt vmcnt(3)
	v_mov_b32_e32 v60, v75
	v_mov_b32_e32 v61, v76
	v_mov_b32_e32 v75, v77
	v_pk_add_f32 v[60:61], v[60:61], v[74:75]
	s_nop 0
	v_add_f32_e32 v60, v60, v61
	s_waitcnt vmcnt(2)
	v_mfma_f32_32x32x16_bf16 v[36:51], v[70:73], v[66:69], v[36:51]
	ds_read_b128 v[70:73], v3 offset:14336
	ds_read_b128 v[78:81], v3 offset:15360
	v_fmamk_f32 v60, v60, 0x3b800000, v222
	v_mul_f32_e32 v61, 0x4b800000, v60
	v_cmp_gt_f32_e32 vcc, s39, v60
	s_nop 1
	v_cndmask_b32_e32 v60, v60, v61, vcc
	s_waitcnt vmcnt(1) lgkmcnt(1)
	v_mfma_f32_32x32x16_bf16 v[36:51], v[70:73], v[62:65], v[36:51]
	v_rsq_f32_e32 v94, v60
	v_mfma_f32_32x32x16_bf16 v[20:35], v[82:85], v[66:69], v[20:35]
	s_waitcnt vmcnt(0) lgkmcnt(0)
	v_mfma_f32_32x32x16_bf16 v[36:51], v[78:81], v[56:59], v[36:51]
	ds_read_b128 v[70:73], v3 offset:30720
	ds_read_b128 v[74:77], v3 offset:31744
	ds_read_b128 v[78:81], v3 offset:47104
	ds_read_b128 v[90:93], v3 offset:48128
	v_mul_f32_e32 v3, 0x45800000, v94
	v_cndmask_b32_e32 v3, v94, v3, vcc
	s_nop 5
	v_mul_f32_e32 v95, v37, v37
	s_waitcnt lgkmcnt(3)
	v_mfma_f32_32x32x16_bf16 v[20:35], v[70:73], v[62:65], v[20:35]
	v_fmac_f32_e32 v95, v36, v36
	v_fmac_f32_e32 v95, v38, v38
	v_fmac_f32_e32 v95, v39, v39
	v_fmac_f32_e32 v95, v40, v40
	v_fmac_f32_e32 v95, v41, v41
	v_fmac_f32_e32 v95, v42, v42
	s_waitcnt lgkmcnt(2)
	v_mfma_f32_32x32x16_bf16 v[20:35], v[74:77], v[56:59], v[20:35]
	v_fmac_f32_e32 v95, v43, v43
	v_fmac_f32_e32 v95, v44, v44
	v_fmac_f32_e32 v95, v45, v45
	v_fmac_f32_e32 v95, v46, v46
	v_fmac_f32_e32 v95, v47, v47
	v_fmac_f32_e32 v95, v48, v48
	v_mfma_f32_32x32x16_bf16 v[4:19], v[86:89], v[66:69], v[4:19]
	v_fmac_f32_e32 v95, v49, v49
	v_fmac_f32_e32 v95, v50, v50
	v_fmac_f32_e32 v95, v51, v51
	v_fmac_f32_e32 v95, v20, v20
	v_fmac_f32_e32 v95, v21, v21
	v_fmac_f32_e32 v95, v22, v22
	s_waitcnt lgkmcnt(1)
	v_mfma_f32_32x32x16_bf16 v[4:19], v[78:81], v[62:65], v[4:19]
	v_fmac_f32_e32 v95, v23, v23
	v_fmac_f32_e32 v95, v24, v24
	v_fmac_f32_e32 v95, v25, v25
	v_fmac_f32_e32 v95, v26, v26
	v_fmac_f32_e32 v95, v27, v27
	v_fmac_f32_e32 v95, v28, v28
	s_waitcnt lgkmcnt(0)
	v_mfma_f32_32x32x16_bf16 v[4:19], v[90:93], v[56:59], v[4:19]
	v_fmac_f32_e32 v95, v29, v29
	v_fmac_f32_e32 v95, v30, v30
	v_fmac_f32_e32 v95, v31, v31
	v_fmac_f32_e32 v95, v32, v32
	v_fmac_f32_e32 v95, v33, v33
	v_fmac_f32_e32 v95, v34, v34
	v_fmac_f32_e32 v95, v35, v35
	s_nop 4
	v_fmac_f32_e32 v95, v4, v4
	v_fmac_f32_e32 v95, v5, v5
	v_fmac_f32_e32 v95, v6, v6
	v_fmac_f32_e32 v95, v7, v7
	v_fmac_f32_e32 v95, v8, v8
	v_fmac_f32_e32 v95, v9, v9
	v_fmac_f32_e32 v95, v10, v10
	v_fmac_f32_e32 v95, v11, v11
	v_fmac_f32_e32 v95, v12, v12
	v_fmac_f32_e32 v95, v13, v13
	v_fmac_f32_e32 v95, v14, v14
	v_fmac_f32_e32 v95, v15, v15
	v_pk_mul_f32 v[82:83], v[16:17], v[16:17]
	v_pk_mul_f32 v[64:65], v[18:19], v[18:19]
	v_add_f32_e32 v82, v82, v95
	v_add_f32_e32 v82, v83, v82
	v_add_f32_e32 v64, v64, v82
	v_add_f32_e32 v64, v65, v64
	v_mov_b32_e32 v65, v64
	s_nop 1
	v_permlane32_swap_b32_e32 v64, v65
	v_add_f32_e32 v64, v64, v65
	v_mul_f32_e32 v64, v3, v64
	v_mul_f32_e32 v64, v3, v64
	v_fmamk_f32 v64, v64, 0x3c2aaaab, v222
	v_mul_f32_e32 v65, 0x4b800000, v64
	v_cmp_gt_f32_e32 vcc, s39, v64
	v_cndmask_b32_e32 v64, v64, v65, vcc
	v_rsq_f32_e32 v110, v64
	v_mul_f32_e32 v53, 0x45800000, v110
	v_cndmask_b32_e32 v53, v110, v53, vcc
	v_mul_f32_e32 v53, 0x3e16c740, v53
	v_mul_f32_e32 v110, v3, v53
	s_waitcnt vmcnt(0)
; __device__ __forceinline__ bf16x8 pk8(const f32x16& p, int b) { u32x4 w; w.x = cvt_pk_bf16(p[b], p[b + 1]); w.y = cvt_pk_bf16(p[b + 2], p[b + 3]); w.z = cvt_pk_bf16(p[b + 4], p[b + 5]); w.w = cvt_pk_bf16(p[b + 6], p[b + 7]); return __builtin_bit_cast(bf16x8, w); }
; template <bool FOX>
; __device__ __forceinline__ void attn_unit(const Args& A, int b, int h, int qb, LAS char* shm, LAS float* dg) {
;     ...
;             const float sc = rsqrtf(ss * (1.f / 96.f) + EPS) * C2_MLA * rq;
; #pragma unroll
;             for (int blk = 0; blk < 3; ++blk)
; #pragma unroll
;                 for (int g = 0; g < 4; ++g) { const f32x4 gg = *(const f32x4*)(A.gmq + 32 * blk + 8 * g + 4 * hi);
; #pragma unroll
;                     for (int i = 0; i < 4; ++i) qa[blk][4 * g + i] *= sc * gg[i]; }
; #pragma unroll
;             for (int e = 0; e < 2; ++e) { const f32x4 c = *(const f32x4*)(A.cosT + row * 16 + 8 * e + 4 * hi), sn = *(const f32x4*)(A.sinT + row * 16 + 8 * e + 4 * hi);
; #pragma unroll
;                 for (int i = 0; i < 4; ++i) { const float x1 = qa[2][4 * e + i], x2 = qa[2][8 + 4 * e + i]; qa[2][4 * e + i] = x1 * c[i] - x2 * sn[i]; qa[2][8 + 4 * e + i] = x2 * c[i] + x1 * sn[i]; } }
; #pragma unroll
;             for (int blk = 0; blk < 3; ++blk) { qr[2 * blk] = pk8(qa[blk], 0); qr[2 * blk + 1] = pk8(qa[blk], 8); }
	v_mul_f32_e32 v3, v162, v110
	v_mul_f32_e32 v3, v36, v3
	v_mul_f32_e32 v36, v163, v110
	v_mul_f32_e32 v53, v37, v36
	v_mul_f32_e32 v36, v164, v110
	v_mul_f32_e32 v70, v38, v36
	v_mul_f32_e32 v36, v165, v110
	v_mul_f32_e32 v71, v39, v36
	v_mul_f32_e32 v36, v166, v110
	v_mul_f32_e32 v72, v40, v36
	v_mul_f32_e32 v36, v167, v110
	v_mul_f32_e32 v73, v41, v36
	v_mul_f32_e32 v36, v168, v110
	v_mul_f32_e32 v74, v42, v36
	v_mul_f32_e32 v36, v169, v110
	v_mul_f32_e32 v75, v43, v36
	v_mul_f32_e32 v36, v170, v110
	v_mul_f32_e32 v66, v44, v36
	v_mul_f32_e32 v36, v171, v110
	v_mul_f32_e32 v67, v45, v36
	v_mul_f32_e32 v36, v172, v110
	v_mul_f32_e32 v68, v46, v36
	v_mul_f32_e32 v36, v173, v110
	v_mul_f32_e32 v69, v47, v36
	v_mul_f32_e32 v36, v174, v110
	v_mul_f32_e32 v48, v48, v36
	v_mul_f32_e32 v36, v175, v110
	v_mul_f32_e32 v49, v49, v36
	v_mul_f32_e32 v36, v176, v110
	v_mul_f32_e32 v50, v50, v36
	v_mul_f32_e32 v36, v177, v110
	v_mul_f32_e32 v51, v51, v36
	v_mul_f32_e32 v36, v178, v110
	v_mul_f32_e32 v60, v20, v36
	v_mul_f32_e32 v20, v179, v110
	v_mul_f32_e32 v61, v21, v20
	v_mul_f32_e32 v20, v180, v110
	v_mul_f32_e32 v52, v22, v20
	v_mul_f32_e32 v20, v181, v110
	v_mul_f32_e32 v62, v23, v20
	s_and_b64 vcc, exec, s[24:25]
	v_cvt_pk_bf16_f32 v138, v3, v53
	v_cvt_pk_bf16_f32 v139, v70, v71
	v_cvt_pk_bf16_f32 v140, v72, v73
	v_cvt_pk_bf16_f32 v141, v74, v75
	v_cvt_pk_bf16_f32 v142, v66, v67
	v_cvt_pk_bf16_f32 v143, v68, v69
	v_cvt_pk_bf16_f32 v144, v48, v49
	v_cvt_pk_bf16_f32 v145, v50, v51
	v_cvt_pk_bf16_f32 v146, v60, v61
	v_cvt_pk_bf16_f32 v147, v52, v62
	v_mul_f32_e32 v54, v182, v110
	v_mul_f32_e32 v54, v24, v54
	v_mul_f32_e32 v24, v183, v110
	v_mul_f32_e32 v55, v25, v24
	v_mul_f32_e32 v24, v184, v110
	v_mul_f32_e32 v56, v26, v24
	v_mul_f32_e32 v24, v185, v110
	v_mul_f32_e32 v57, v27, v24
	v_mul_f32_e32 v24, v186, v110
	v_mul_f32_e32 v28, v28, v24
	v_mul_f32_e32 v24, v187, v110
	v_mul_f32_e32 v29, v29, v24
	v_mul_f32_e32 v24, v188, v110
	v_mul_f32_e32 v30, v30, v24
	v_mul_f32_e32 v24, v189, v110
	v_mul_f32_e32 v31, v31, v24
	v_mul_f32_e32 v24, v190, v110
	v_mul_f32_e32 v32, v32, v24
	v_mul_f32_e32 v24, v191, v110
	v_mul_f32_e32 v33, v33, v24
	v_mul_f32_e32 v24, v192, v110
	v_mul_f32_e32 v34, v34, v24
	v_mul_f32_e32 v24, v193, v110
	v_mul_f32_e32 v35, v35, v24
	v_mov_b32_e32 v24, v198
	v_mov_b32_e32 v25, v194
	v_pk_mul_f32 v[24:25], v[24:25], v[110:111] op_sel_hi:[1,0]
	v_mov_b32_e32 v26, v12
	v_mov_b32_e32 v27, v4
	v_pk_mul_f32 v[24:25], v[26:27], v[24:25]
	v_mov_b32_e32 v26, v202
	v_mov_b32_e32 v27, v206
	v_pk_mul_f32 v[26:27], v[26:27], v[24:25]
	v_mov_b32_e32 v90, v199
	v_sub_f32_e32 v58, v27, v26
	v_mov_b32_e32 v26, v206
	v_mov_b32_e32 v27, v202
	v_pk_mul_f32 v[24:25], v[26:27], v[24:25]
	v_mov_b32_e32 v4, v13
	v_add_f32_e32 v26, v24, v25
	v_mov_b32_e32 v91, v195
	v_pk_mul_f32 v[24:25], v[90:91], v[110:111] op_sel_hi:[1,0]
	v_mov_b32_e32 v106, v203
	v_pk_mul_f32 v[4:5], v[4:5], v[24:25]
	v_mov_b32_e32 v102, v207
	v_mov_b32_e32 v107, v207
	v_pk_mul_f32 v[12:13], v[106:107], v[4:5]
	v_mov_b32_e32 v103, v203
	v_pk_mul_f32 v[4:5], v[102:103], v[4:5]
	v_sub_f32_e32 v24, v13, v12
	v_add_f32_e32 v25, v4, v5
	v_mov_b32_e32 v4, v200
	v_mov_b32_e32 v5, v196
	v_pk_mul_f32 v[4:5], v[4:5], v[110:111] op_sel_hi:[1,0]
	v_mov_b32_e32 v12, v14
	v_mov_b32_e32 v13, v6
	v_pk_mul_f32 v[4:5], v[12:13], v[4:5]
	v_mov_b32_e32 v12, v204
	v_mov_b32_e32 v13, v208
	v_pk_mul_f32 v[12:13], v[12:13], v[4:5]
	v_mov_b32_e32 v92, v201
	v_sub_f32_e32 v14, v13, v12
	v_mov_b32_e32 v12, v208
	v_mov_b32_e32 v13, v204
	v_pk_mul_f32 v[4:5], v[12:13], v[4:5]
	v_mov_b32_e32 v6, v15
	v_add_f32_e32 v12, v4, v5
	v_mov_b32_e32 v93, v197
	v_pk_mul_f32 v[4:5], v[92:93], v[110:111] op_sel_hi:[1,0]
	v_mov_b32_e32 v108, v205
	v_pk_mul_f32 v[4:5], v[6:7], v[4:5]
	v_mov_b32_e32 v104, v209
	v_mov_b32_e32 v109, v209
	v_pk_mul_f32 v[6:7], v[108:109], v[4:5]
	v_mov_b32_e32 v105, v205
	v_pk_mul_f32 v[4:5], v[104:105], v[4:5]
	v_sub_f32_e32 v13, v7, v6
	v_add_f32_e32 v15, v4, v5
	v_mov_b32_e32 v4, v210
	v_mov_b32_e32 v5, v214
	v_pk_mul_f32 v[4:5], v[4:5], v[110:111] op_sel_hi:[1,0]
	v_mov_b32_e32 v6, v16
	v_mov_b32_e32 v7, v8
	v_pk_mul_f32 v[4:5], v[6:7], v[4:5]
	v_mov_b32_e32 v6, v218
	v_mov_b32_e32 v7, v112
	v_pk_mul_f32 v[6:7], v[4:5], v[6:7]
	v_mov_b32_e32 v40, v211
	v_sub_f32_e32 v16, v7, v6
	v_mov_b32_e32 v6, v112
	v_mov_b32_e32 v7, v218
	v_pk_mul_f32 v[4:5], v[4:5], v[6:7]
	v_mov_b32_e32 v8, v17
	v_add_f32_e32 v27, v4, v5
	v_mov_b32_e32 v41, v215
	v_pk_mul_f32 v[4:5], v[40:41], v[110:111] op_sel_hi:[1,0]
	v_mov_b32_e32 v44, v219
	v_pk_mul_f32 v[4:5], v[8:9], v[4:5]
	v_mov_b32_e32 v20, v113
	v_mov_b32_e32 v45, v113
	v_pk_mul_f32 v[6:7], v[4:5], v[44:45]
	v_mov_b32_e32 v21, v219
	v_pk_mul_f32 v[4:5], v[4:5], v[20:21]
	v_sub_f32_e32 v8, v7, v6
	v_add_f32_e32 v9, v4, v5
	v_mov_b32_e32 v4, v212
	v_mov_b32_e32 v5, v216
	v_pk_mul_f32 v[4:5], v[4:5], v[110:111] op_sel_hi:[1,0]
	v_mov_b32_e32 v6, v18
	v_mov_b32_e32 v7, v10
	v_pk_mul_f32 v[4:5], v[6:7], v[4:5]
	v_mov_b32_e32 v6, v220
	v_mov_b32_e32 v7, v114
	v_pk_mul_f32 v[6:7], v[4:5], v[6:7]
	v_mov_b32_e32 v42, v213
	v_sub_f32_e32 v17, v7, v6
	v_mov_b32_e32 v6, v114
	v_mov_b32_e32 v7, v220
	v_pk_mul_f32 v[4:5], v[4:5], v[6:7]
	v_mov_b32_e32 v10, v19
	v_add_f32_e32 v18, v4, v5
	v_mov_b32_e32 v43, v217
	v_pk_mul_f32 v[4:5], v[42:43], v[110:111] op_sel_hi:[1,0]
	v_mov_b32_e32 v46, v221
	v_pk_mul_f32 v[4:5], v[10:11], v[4:5]
	v_mov_b32_e32 v22, v115
	v_mov_b32_e32 v47, v115
	v_pk_mul_f32 v[6:7], v[4:5], v[46:47]
	v_mov_b32_e32 v23, v221
	v_pk_mul_f32 v[4:5], v[4:5], v[22:23]
	v_sub_f32_e32 v6, v7, v6
	v_add_f32_e32 v4, v4, v5
	v_cvt_pk_bf16_f32 v148, v54, v55
	v_cvt_pk_bf16_f32 v149, v56, v57
	v_cvt_pk_bf16_f32 v150, v28, v29
	v_cvt_pk_bf16_f32 v151, v30, v31
	v_cvt_pk_bf16_f32 v152, v32, v33
	v_cvt_pk_bf16_f32 v153, v34, v35
	v_cvt_pk_bf16_f32 v154, v58, v24
	v_cvt_pk_bf16_f32 v155, v14, v13
	v_cvt_pk_bf16_f32 v156, v16, v8
	v_cvt_pk_bf16_f32 v157, v17, v6
	v_cvt_pk_bf16_f32 v158, v26, v25
	v_cvt_pk_bf16_f32 v159, v12, v15
	v_cvt_pk_bf16_f32 v160, v27, v9
	v_cvt_pk_bf16_f32 v161, v18, v4
	s_cbranch_vccz .LBB0_817
	s_waitcnt vmcnt(6)
	s_mov_b64 s[42:43], 0
